# speedup vs baseline: 1.0025x; 1.0025x over previous
.Lj_loop:
	s_and_b32 s70, s20, 1
	s_waitcnt lgkmcnt(0)
	s_barrier
	s_mul_i32 s38, s70, 0x1100
	s_lshl_b32 s10, s70, 13
	s_add_i32 s14, s10, s34
	s_mov_b32 s15, 0
	v_lshl_add_u64 v[244:245], v[192:193], 0, s[14:15]
	s_add_i32 s14, s10, s30
	v_lshl_add_u64 v[246:247], v[192:193], 0, s[14:15]
	s_add_i32 s14, s10, s28
	v_lshl_add_u64 v[248:249], v[192:193], 0, s[14:15]
	s_cmp_eq_u32 s20, 0
	s_cbranch_scc1 .Lj_nopollE
	global_load_dwordx2 v[214:215], v[244:245], off sc1
	global_load_dwordx2 v[210:211], v[246:247], off sc1
	global_load_dwordx2 v[212:213], v[248:249], off sc1
.Lj_nopollE:
	v_add_u32_e32 v229, s38, v222
	v_add_u32_e32 v230, s43, v229
	ds_read_b128 v[150:153], v230 offset:0
	ds_read_b128 v[194:197], v230 offset:128
	ds_read_b128 v[198:201], v230 offset:256
	ds_read_b128 v[232:235], v230 offset:384
	s_xor_b32 s83, s70, 1
	s_lshl_b32 s83, s83, 4
	s_add_i32 s83, s83, 0x26a20
	v_mov_b32_e32 v239, s83
	ds_read_b128 v[240:243], v239
	s_cmp_lg_u32 s20, 1
	s_cselect_b64 s[10:11], -1, 0
	s_and_b64 s[14:15], s[10:11], s[26:27]
	s_and_saveexec_b64 s[10:11], s[14:15]
	s_cbranch_execz .Lj_norr
	s_lshl_b32 s14, s70, 4
	s_or_b32 s14, s14, 0x26a00
	v_mov_b32_e32 v236, s14
	s_add_i32 s14, s20, -2
	ds_read_b128 v[236:239], v236
	s_cmp_lg_u32 s20, 0
	s_cselect_b32 s14, s14, 0x64
	s_ashr_i32 s15, s14, 31
	s_add_u32 s14, s22, s14
	s_addc_u32 s15, s23, s15
	s_lshl_b64 s[14:15], s[14:15], 4
	s_add_u32 s14, s24, s14
	s_addc_u32 s15, s25, s15
	s_waitcnt lgkmcnt(0)
	v_add_f32_e32 v236, v236, v237
	v_add_f32_e32 v238, v238, v239
	v_add_f32_e32 v236, v236, v238
	global_store_dword v191, v236, s[14:15]

.Lj_nostop:
	v_mov_b64_e32 v[146:147], 0
	v_mov_b64_e32 v[148:149], 0
	v_mov_b64_e32 v[154:155], 0
	v_mov_b64_e32 v[156:157], 0
	v_mov_b64_e32 v[158:159], 0
	v_mov_b64_e32 v[160:161], 0
	v_mov_b64_e32 v[162:163], 0
	v_mov_b64_e32 v[164:165], 0
	v_mov_b32_e32 v231, 0
	v_smfmac_f32_16x16x64_bf16 v[162:165], v[150:153], v[166:173], v223
	ds_read_b128 v[166:169], v224 offset:6144
	v_smfmac_f32_16x16x64_bf16 v[146:149], v[150:153], v[2:9], v223
	ds_read_b128 v[170:173], v224 offset:7168
	v_smfmac_f32_16x16x64_bf16 v[154:157], v[150:153], v[18:25], v223
	v_smfmac_f32_16x16x64_bf16 v[158:161], v[150:153], v[34:41], v223
	s_cmp_eq_u32 s20, 0
	s_cbranch_scc1 .Lj_nopoll0
	s_waitcnt vmcnt(4)
	global_load_dwordx2 v[204:205], v[244:245], off sc1
	global_load_dwordx2 v[202:203], v[246:247], off sc1
	global_load_dwordx2 v[218:219], v[248:249], off sc1
.Lj_nopoll0:
	v_smfmac_f32_16x16x64_bf16 v[162:165], v[194:197], v[174:181], v223
	ds_read_b128 v[174:177], v224 offset:8192
	v_smfmac_f32_16x16x64_bf16 v[146:149], v[194:197], v[10:17], v223
	ds_read_b128 v[178:181], v224 offset:9216
	v_smfmac_f32_16x16x64_bf16 v[154:157], v[194:197], v[26:33], v223
	v_smfmac_f32_16x16x64_bf16 v[158:161], v[194:197], v[42:49], v223
	v_smfmac_f32_16x16x64_bf16 v[162:165], v[198:201], v[182:189], v223
	ds_read_b128 v[182:185], v224 offset:10240
	v_smfmac_f32_16x16x64_bf16 v[146:149], v[198:201], v[50:57], v223
	ds_read_b128 v[186:189], v224 offset:11264
	v_smfmac_f32_16x16x64_bf16 v[154:157], v[198:201], v[66:73], v223
	v_smfmac_f32_16x16x64_bf16 v[158:161], v[198:201], v[82:89], v223
	s_waitcnt lgkmcnt(4)
	v_smfmac_f32_16x16x64_bf16 v[162:165], v[232:235], v[166:173], v223
	ds_read_b128 v[166:169], v224 offset:12288
	v_smfmac_f32_16x16x64_bf16 v[146:149], v[232:235], v[58:65], v223
	ds_read_b128 v[170:173], v224 offset:13312
	v_smfmac_f32_16x16x64_bf16 v[154:157], v[232:235], v[74:81], v223
	v_smfmac_f32_16x16x64_bf16 v[158:161], v[232:235], v[90:97], v223
	s_cmp_eq_u32 s20, 0
	s_cbranch_scc1 .Lj_gdone
	s_mov_b32 s29, 0
	s_waitcnt vmcnt(3)
	v_cmp_eq_u32_e32 vcc, s20, v215
	v_cmp_eq_u32_e64 s[14:15], s20, v211
	v_cmp_eq_u32_e64 s[72:73], s20, v213
	s_and_b64 vcc, vcc, s[14:15]
	s_and_b64 vcc, vcc, s[72:73]
	s_cmp_eq_u64 vcc, exec
	s_cbranch_scc1 .Lj_got1

.Lj_got1:
	v_cvt_pk_bf16_f32 v236, v214, v214
	v_lshlrev_b32_e32 v237, 16, v236
	v_sub_f32_e32 v237, v214, v237
	v_add_u32_e32 v238, s38, v225
	v_cvt_pk_bf16_f32 v237, v237, v237
	ds_write_b16 v238, v236
	ds_write_b16 v238, v237 offset:2176
	v_cvt_pk_bf16_f32 v244, v210, v210
	v_lshlrev_b32_e32 v245, 16, v244
	v_sub_f32_e32 v245, v210, v245
	v_add_u32_e32 v238, s38, v226
	v_cvt_pk_bf16_f32 v245, v245, v245
	ds_write_b16 v238, v244
	ds_write_b16 v238, v245 offset:2176
	v_cvt_pk_bf16_f32 v246, v212, v212
	v_lshlrev_b32_e32 v247, 16, v246
	v_sub_f32_e32 v247, v212, v247
	v_add_u32_e32 v238, s38, v227
	v_cvt_pk_bf16_f32 v247, v247, v247
	ds_write_b16 v238, v246
	ds_write_b16 v238, v247 offset:2176
	s_branch .Lj_gdone
